# hg_a: lower-bound table hoisted out of the chunk loop into free VGPRs; chunk-top vmcnt(0) moved to the first read of the prefetched registers
# speedup vs baseline: 1.1387x; 1.0058x over previous
; template <bool WITHO, bool RAW = false>
; __device__ __forceinline__ void hg_pass(const Frame& F, const bf16_t* P, const float* lbh, int b, int h, int nb, int dir, f32x4 (&S)[4][4], float (&Gsum)[16],
;                                         LAS bf16_t* Vl, LAS bf16_t* Kl, float* OF, const float* ngp) {
;     const int tau = F.lane & 15, g = F.lane >> 4;
;     const unsigned vaddr = (unsigned)(size_t)Vl + (unsigned)((4 * g + (tau >> 2)) * 128 + (tau & 3) * 8);
;     const unsigned kaddr = (unsigned)(size_t)Kl + (unsigned)((4 * g + (tau >> 2)) * 128 + (tau & 3) * 8);
;     u32x2 zr[4], vr[4], qr[4];
;     float ngv[4] = {0.f, 0.f, 0.f, 0.f};
;     if (WITHO && !RAW && dir) {
; #pragma unroll
;         for (int vt = 0; vt < 4; ++vt) ngv[vt] = ngp[16 * vt + tau]; }
;     { const int t = dir ? (HG_U - 1 - tau) : tau; const bf16_t* pr = P + (size_t)hg_row(b, nb, t) * 4096 + h * 64 + 4 * g;
; #pragma unroll
;       for (int m = 0; m < 4; ++m) { zr[m] = *(const u32x2*)(pr + (dir ? 2560 : 2048) + 16 * m); vr[m] = *(const u32x2*)(pr + 3072 + 16 * m); } }
;     for (int ci = 0; ci < HG_U / 16; ++ci) {
;         float kk[16], c[16];
;         if (WITHO) { const int pos = ci * 16 + tau, t = dir ? (HG_U - 1 - pos) : pos; const bf16_t* pr = P + (size_t)hg_row(b, nb, t) * 4096 + h * 64 + 4 * g;
; #pragma unroll
;             for (int m = 0; m < 4; ++m) qr[m] = *(const u32x2*)(pr + 1536 + 16 * m); }
; #pragma unroll
;         for (int m = 0; m < 4; ++m) { const float z0 = __uint_as_float(zr[m].x << 16), z1 = __uint_as_float(zr[m].x & 0xffff0000u), z2 = __uint_as_float(zr[m].y << 16), z3 = __uint_as_float(zr[m].y & 0xffff0000u);
;             const float zz[4] = {z0, z1, z2, z3};
;             const f32x4 lb4 = *(const f32x4*)(lbh + 16 * m + 4 * g);
; #pragma unroll
;             for (int i = 0; i < 4; ++i) { const float lb = lb4[i]; const float f = fmaxf(lb + (1.0f - lb) * sigmoidf_(zz[i]), 1e-30f); kk[m * 4 + i] = 1.0f - f; c[m * 4 + i] = __logf(f); }
; __device__ __forceinline__ void ph_hg_a(const Frame& F, int j) {
;     ...
;         const int dir = task & 1, nb = 2 + (task >> 1) % (HG_NU - 2), bh = (task >> 1) / (HG_NU - 2), b = bh >> 3, h = bh & 7;
;         const float* lbh = (const float*)(F.ws + OFF_LBT) + (j * 2 + dir) * 512 + h * 64;
;         f32x4 S[4][4];
; #pragma unroll
;         for (int kt = 0; kt < 4; ++kt)
; #pragma unroll
.LBB0_688:
	s_ashr_i32 s6, s16, 6
	v_add_u32_e32 v0, s20, v142
	s_lshl_b32 s7, s6, 6
	v_ashrrev_i32_e32 v1, 31, v0
	s_and_b32 s7, s7, 0x1c0
	v_lshlrev_b64 v[0:1], 13, v[0:1]
	v_lshl_add_u64 v[0:1], s[82:83], 0, v[0:1]
	s_lshl_b32 s16, s7, 1
	s_mov_b32 s17, s65
	v_lshl_add_u64 v[0:1], v[0:1], 0, s[16:17]
	v_readlane_b32 s14, v251, 47
	v_lshl_add_u64 v[0:1], v[84:85], 1, v[0:1]
	s_lshl_b32 s64, s14, 1
	v_lshl_add_u64 v[4:5], v[0:1], 0, s[64:65]
	v_add_co_u32_e32 v6, vcc, s97, v0
	s_lshl_b32 s20, s7, 2
	s_nop 0
	v_addc_co_u32_e32 v7, vcc, 0, v1, vcc
	global_load_dwordx2 v[134:135], v[4:5], off
	global_load_dwordx2 v[132:133], v[4:5], off offset:32
	global_load_dwordx2 v[130:131], v[4:5], off offset:64
	global_load_dwordx2 v[0:1], v[4:5], off offset:96
	global_load_dwordx2 v[114:115], v[6:7], off offset:2048
	global_load_dwordx2 v[116:117], v[6:7], off offset:2080
	global_load_dwordx2 v[118:119], v[6:7], off offset:2112
	global_load_dwordx2 v[120:121], v[6:7], off offset:2144
	s_add_i32 s7, s10, s13
	s_addk_i32 s7, 0x300
	s_mov_b32 s21, s65
	s_and_b64 s[4:5], s[4:5], exec
	v_mov_b32_e32 v4, 0
	v_lshl_add_u64 v[110:111], v[86:87], 0, s[20:21]
	global_load_dwordx4 v[192:195], v[110:111], off
	global_load_dwordx4 v[196:199], v[110:111], off offset:64
	global_load_dwordx4 v[200:203], v[110:111], off offset:128
	global_load_dwordx4 v[204:207], v[110:111], off offset:192
	v_lshl_add_u64 v[112:113], v[88:89], 0, s[16:17]
	s_cselect_b32 s4, s11, s7
	s_movk_i32 s5, 0x6f
	v_mov_b32_e32 v147, v145
	v_mov_b32_e32 v5, v4
	v_mov_b32_e32 v6, v4
	v_mov_b32_e32 v7, v4
	v_mov_b32_e32 v8, v4
	v_mov_b32_e32 v9, v4
	v_mov_b32_e32 v10, v4
	v_mov_b32_e32 v11, v4
	v_mov_b32_e32 v12, v4
	v_mov_b32_e32 v13, v4
	v_mov_b32_e32 v14, v4
	v_mov_b32_e32 v15, v4
	v_mov_b32_e32 v16, v4
	v_mov_b32_e32 v17, v4
	v_mov_b32_e32 v18, v4
	v_mov_b32_e32 v19, v4
	s_waitcnt vmcnt(0)
	v_mov_b32_e32 v24, v4
	v_mov_b32_e32 v25, v4
	v_mov_b32_e32 v26, v4
	v_mov_b32_e32 v27, v4
	v_mov_b32_e32 v20, v4
	v_mov_b32_e32 v21, v4
	v_mov_b32_e32 v22, v4
	v_mov_b32_e32 v23, v4
	v_mov_b32_e32 v28, v4
	v_mov_b32_e32 v29, v4
	v_mov_b32_e32 v30, v4
	v_mov_b32_e32 v31, v4
	v_mov_b32_e32 v32, v4
	v_mov_b32_e32 v33, v4
	v_mov_b32_e32 v34, v4
	v_mov_b32_e32 v35, v4
	v_mov_b32_e32 v40, v4
	v_mov_b32_e32 v41, v4
	v_mov_b32_e32 v42, v4
	v_mov_b32_e32 v43, v4
	v_mov_b32_e32 v36, v4
	v_mov_b32_e32 v37, v4
	v_mov_b32_e32 v38, v4
	v_mov_b32_e32 v39, v4
	v_mov_b32_e32 v44, v4
	v_mov_b32_e32 v45, v4
	v_mov_b32_e32 v46, v4
	v_mov_b32_e32 v47, v4
	v_mov_b32_e32 v48, v4
	v_mov_b32_e32 v49, v4
	v_mov_b32_e32 v50, v4
	v_mov_b32_e32 v51, v4
	v_mov_b32_e32 v56, v4
	v_mov_b32_e32 v57, v4
	v_mov_b32_e32 v58, v4
	v_mov_b32_e32 v59, v4
	v_mov_b32_e32 v52, v4
	v_mov_b32_e32 v53, v4
	v_mov_b32_e32 v54, v4
	v_mov_b32_e32 v55, v4
	v_mov_b32_e32 v60, v4
	v_mov_b32_e32 v61, v4
	v_mov_b32_e32 v62, v4
	v_mov_b32_e32 v63, v4
	v_mov_b32_e32 v64, v4
	v_mov_b32_e32 v65, v4
	v_mov_b32_e32 v66, v4
	v_mov_b32_e32 v67, v4
	v_mov_b32_e32 v94, v4
	v_mov_b32_e32 v95, v4
	v_mov_b32_e32 v96, v4
	v_mov_b32_e32 v97, v4
	v_mov_b32_e32 v98, v4
	v_mov_b32_e32 v99, v4
	v_mov_b32_e32 v100, v4
	v_mov_b32_e32 v101, v4
	v_mov_b32_e32 v102, v4
	v_mov_b32_e32 v103, v4
	v_mov_b32_e32 v104, v4
	v_mov_b32_e32 v105, v4
	v_mov_b32_e32 v106, v4
	v_mov_b32_e32 v107, v4
	v_mov_b32_e32 v108, v4
	v_mov_b32_e32 v109, v4
	v_mov_b64_e32 v[122:123], v[134:135]
	s_waitcnt lgkmcnt(0)
	v_mov_b64_e32 v[124:125], v[132:133]
	v_mov_b64_e32 v[126:127], v[130:131]
	v_mov_b64_e32 v[128:129], v[0:1]
	s_branch .LBB0_690
.LBB0_689:
	v_lshlrev_b32_e32 v3, 16, v134
	v_mul_f32_e32 v3, 0xbfb8aa3b, v3
	v_exp_f32_e32 v3, v3
	v_sub_f32_e32 v137, 1.0, v192
	v_and_b32_e32 v134, 0xffff0000, v134
	v_mul_f32_e32 v134, 0xbfb8aa3b, v134
	v_add_f32_e32 v3, 1.0, v3
	v_rcp_f32_e32 v3, v3
	v_exp_f32_e32 v134, v134
	v_lshlrev_b32_e32 v136, 16, v135
	v_mul_f32_e32 v136, 0xbfb8aa3b, v136
	v_fma_f32 v3, v137, v3, v192
	v_max_f32_e32 v3, 0xda24260, v3
	v_add_f32_e32 v134, 1.0, v134
	v_rcp_f32_e32 v134, v134
	v_log_f32_e32 v80, v3
	v_exp_f32_e32 v136, v136
	v_and_b32_e32 v135, 0xffff0000, v135
	v_mul_f32_e32 v135, 0xbfb8aa3b, v135
	v_mul_f32_e32 v137, 0x3f317217, v80
	v_fma_f32 v137, v80, s93, -v137
	v_fmac_f32_e32 v137, 0x3377d1cf, v80
	v_fmac_f32_e32 v137, 0x3f317217, v80
	v_add_f32_e32 v136, 1.0, v136
	v_rcp_f32_e32 v136, v136
	v_mov_b32_e32 v80, v137
	v_sub_f32_e32 v137, 1.0, v193
	v_fma_f32 v81, v137, v134, v193
	v_max_f32_e32 v81, 0xda24260, v81
	v_mov_b32_e32 v148, v80
	v_log_f32_e32 v134, v81
	v_sub_f32_e32 v80, 1.0, v81
	v_exp_f32_e32 v135, v135
	v_sub_f32_e32 v3, 1.0, v3
	v_mul_f32_e32 v81, 0x3f317217, v134
	v_fma_f32 v81, v134, s93, -v81
	v_fmac_f32_e32 v81, 0x3377d1cf, v134
	v_fmac_f32_e32 v81, 0x3f317217, v134
	v_add_f32_e32 v135, 1.0, v135
	v_rcp_f32_e32 v135, v135
	v_sub_f32_e32 v134, 1.0, v194
	v_fma_f32 v82, v134, v136, v194
	v_max_f32_e32 v82, 0xda24260, v82
	v_mov_b32_e32 v149, v81
	v_log_f32_e32 v134, v82
	v_sub_f32_e32 v81, 1.0, v82
	s_add_i32 s5, s5, -16
	v_add_u32_e32 v147, 16, v147
	v_mul_f32_e32 v82, 0x3f317217, v134
	v_fma_f32 v82, v134, s93, -v82
	v_fmac_f32_e32 v82, 0x3377d1cf, v134
	v_fmac_f32_e32 v82, 0x3f317217, v134
	s_cmpk_lg_i32 s5, 0xffef
	s_nop 0
	v_sub_f32_e32 v134, 1.0, v195
	v_fma_f32 v83, v134, v135, v195
	v_max_f32_e32 v83, 0xda24260, v83
	v_mov_b32_e32 v150, v82
	v_lshlrev_b32_e32 v135, 16, v132
	v_log_f32_e32 v134, v83
	v_mul_f32_e32 v135, 0xbfb8aa3b, v135
	v_exp_f32_e32 v135, v135
	v_sub_f32_e32 v82, 1.0, v83
	v_mul_f32_e32 v83, 0x3f317217, v134
	v_fma_f32 v83, v134, s93, -v83
	v_add_f32_e32 v135, 1.0, v135
	v_fmac_f32_e32 v83, 0x3377d1cf, v134
	v_rcp_f32_e32 v135, v135
; #define LAS __attribute__((address_space(3)))
; __device__ __forceinline__ float sigmoidf_(float x) { return __builtin_amdgcn_rcpf(1.0f + __expf(-x)); }
; template <int CTRL> __device__ __forceinline__ float dpp_add0(float x) { return x + dppf<CTRL>(0.0f, x); }
; template <bool WITHO, bool RAW = false>
; __device__ __forceinline__ void hg_pass(const Frame& F, const bf16_t* P, const float* lbh, int b, int h, int nb, int dir, f32x4 (&S)[4][4], float (&Gsum)[16],
;                                         LAS bf16_t* Vl, LAS bf16_t* Kl, float* OF, const float* ngp) {
;     ...
;         for (int m = 0; m < 4; ++m) { const float z0 = __uint_as_float(zr[m].x << 16), z1 = __uint_as_float(zr[m].x & 0xffff0000u), z2 = __uint_as_float(zr[m].y << 16), z3 = __uint_as_float(zr[m].y & 0xffff0000u);
;             const float zz[4] = {z0, z1, z2, z3};
;             const f32x4 lb4 = *(const f32x4*)(lbh + 16 * m + 4 * g);
; #pragma unroll
;             for (int i = 0; i < 4; ++i) { const float lb = lb4[i]; const float f = fmaxf(lb + (1.0f - lb) * sigmoidf_(zz[i]), 1e-30f); kk[m * 4 + i] = 1.0f - f; c[m * 4 + i] = __logf(f); }
;             *(LAS u32x2*)(Vl + tau * 64 + 16 * m + 4 * g) = vr[m];
;  }
;         if (ci + 1 < HG_U / 16) { const int pos = (ci + 1) * 16 + tau, t = dir ? (HG_U - 1 - pos) : pos; const bf16_t* pr = P + (size_t)hg_row(b, nb, t) * 4096 + h * 64 + 4 * g;
; #pragma unroll
;             for (int m = 0; m < 4; ++m) { zr[m] = *(const u32x2*)(pr + (dir ? 2560 : 2048) + 16 * m); vr[m] = *(const u32x2*)(pr + 3072 + 16 * m); } }
;         float G[16];
; #pragma unroll
;         for (int q = 0; q < 16; ++q) G[q] = c[q];
; #pragma unroll
;         for (int q = 0; q < 16; q += 4) ROW_ALLREDUCE4(G[q], G[q + 1], G[q + 2], G[q + 3]);
; #pragma unroll
;         for (int q = 0; q < 16; ++q) { c[q] = dpp_add0<0x111>(c[q]); c[q] = dpp_add0<0x112>(c[q]); c[q] = dpp_add0<0x114>(c[q]); c[q] = dpp_add0<0x118>(c[q]); }
	v_fmac_f32_e32 v83, 0x3f317217, v134
	v_and_b32_e32 v132, 0xffff0000, v132
	v_mul_f32_e32 v132, 0xbfb8aa3b, v132
	v_sub_f32_e32 v134, 1.0, v196
	v_fma_f32 v76, v135, v134, v196
	v_max_f32_e32 v76, 0xda24260, v76
	v_exp_f32_e32 v132, v132
	v_lshlrev_b32_e32 v135, 16, v133
	v_log_f32_e32 v134, v76
	v_add_f32_e32 v132, 1.0, v132
	v_rcp_f32_e32 v132, v132
	v_mul_f32_e32 v135, 0xbfb8aa3b, v135
	v_mul_f32_e32 v136, 0x3f317217, v134
	v_fma_f32 v136, v134, s93, -v136
	v_fmac_f32_e32 v136, 0x3377d1cf, v134
	v_fmac_f32_e32 v136, 0x3f317217, v134
	v_exp_f32_e32 v135, v135
	v_and_b32_e32 v133, 0xffff0000, v133
	v_mov_b32_e32 v134, v136
	v_sub_f32_e32 v136, 1.0, v197
	v_fma_f32 v77, v132, v136, v197
	v_max_f32_e32 v77, 0xda24260, v77
	v_mov_b32_e32 v151, v134
	v_log_f32_e32 v132, v77
	v_add_f32_e32 v135, 1.0, v135
	v_rcp_f32_e32 v135, v135
	v_mov_b32_e32 v139, v151
	v_mul_f32_e32 v134, 0x3f317217, v132
	v_fma_f32 v134, v132, s93, -v134
	v_fmac_f32_e32 v134, 0x3377d1cf, v132
	v_fmac_f32_e32 v134, 0x3f317217, v132
	v_add_f32_dpp v151, v151, v151 row_shr:1 row_mask:0xf bank_mask:0xf bound_ctrl:1
	v_sub_f32_e32 v76, 1.0, v76
	v_mov_b32_e32 v132, v134
	v_sub_f32_e32 v134, 1.0, v198
	v_fma_f32 v78, v135, v134, v198
	v_max_f32_e32 v78, 0xda24260, v78
	v_mov_b32_e32 v152, v132
	v_mul_f32_e32 v132, 0xbfb8aa3b, v133
	v_exp_f32_e32 v132, v132
	v_sub_f32_e32 v153, 1.0, v78
	v_log_f32_e32 v134, v78
	v_add_f32_e32 v132, 1.0, v132
	v_rcp_f32_e32 v132, v132
	v_sub_f32_e32 v133, 1.0, v199
	v_mul_f32_e32 v78, 0x3f317217, v134
	v_fma_f32 v78, v134, s93, -v78
	v_fmac_f32_e32 v78, 0x3377d1cf, v134
	v_fma_f32 v79, v132, v133, v199
	v_fmac_f32_e32 v78, 0x3f317217, v134
	v_max_f32_e32 v79, 0xda24260, v79
	v_sub_f32_e32 v155, 1.0, v79
	v_mov_b32_e32 v154, v78
	v_mov_b32_e32 v132, v79
	v_lshlrev_b32_e32 v79, 16, v130
	v_log_f32_e32 v132, v132
	v_mul_f32_e32 v79, 0xbfb8aa3b, v79
	v_exp_f32_e32 v79, v79
	v_mov_b32_e32 v138, v152
	v_mul_f32_e32 v78, 0x3f317217, v132
	v_fma_f32 v78, v132, s93, -v78
	v_add_f32_e32 v79, 1.0, v79
	v_fmac_f32_e32 v78, 0x3377d1cf, v132
	v_rcp_f32_e32 v79, v79
	v_fmac_f32_e32 v78, 0x3f317217, v132
	v_add_f32_dpp v152, v152, v152 row_shr:1 row_mask:0xf bank_mask:0xf bound_ctrl:1
	v_add_f32_dpp v151, v151, v151 row_shr:2 row_mask:0xf bank_mask:0xf bound_ctrl:1
	v_mov_b32_e32 v156, v78
	v_and_b32_e32 v78, 0xffff0000, v130
	v_sub_f32_e32 v130, 1.0, v200
	v_fma_f32 v72, v79, v130, v200
	v_max_f32_e32 v72, 0xda24260, v72
	v_mul_f32_e32 v78, 0xbfb8aa3b, v78
	v_exp_f32_e32 v78, v78
	v_log_f32_e32 v79, v72
	v_add_f32_e32 v78, 1.0, v78
	v_rcp_f32_e32 v78, v78
	v_lshlrev_b32_e32 v130, 16, v131
	v_mul_f32_e32 v132, 0x3f317217, v79
	v_fma_f32 v132, v79, s93, -v132
	v_fmac_f32_e32 v132, 0x3377d1cf, v79
	v_fmac_f32_e32 v132, 0x3f317217, v79
	v_mul_f32_e32 v130, 0xbfb8aa3b, v130
	v_exp_f32_e32 v130, v130
	v_mov_b32_e32 v79, v132
	v_sub_f32_e32 v132, 1.0, v201
	v_fma_f32 v73, v78, v132, v201
	v_max_f32_e32 v73, 0xda24260, v73
	v_mov_b32_e32 v157, v79
	v_log_f32_e32 v78, v73
	v_add_f32_e32 v130, 1.0, v130
	v_rcp_f32_e32 v130, v130
	v_and_b32_e32 v131, 0xffff0000, v131
	v_mul_f32_e32 v79, 0x3f317217, v78
	v_fma_f32 v79, v78, s93, -v79
	v_fmac_f32_e32 v79, 0x3377d1cf, v78
	v_fmac_f32_e32 v79, 0x3f317217, v78
	v_add_f32_dpp v152, v152, v152 row_shr:2 row_mask:0xf bank_mask:0xf bound_ctrl:1
	v_mov_b32_e32 v137, v157
	v_mov_b32_e32 v78, v79
	v_sub_f32_e32 v79, 1.0, v202
	v_fma_f32 v74, v130, v79, v202
	v_max_f32_e32 v74, 0xda24260, v74
	v_mov_b32_e32 v158, v78
	v_mul_f32_e32 v78, 0xbfb8aa3b, v131
	v_log_f32_e32 v79, v74
	v_exp_f32_e32 v78, v78
	v_sub_f32_e32 v159, 1.0, v74
	v_mov_b32_e32 v136, v158
	v_mul_f32_e32 v74, 0x3f317217, v79
	v_add_f32_e32 v78, 1.0, v78
	v_fma_f32 v74, v79, s93, -v74
	v_rcp_f32_e32 v78, v78
	v_fmac_f32_e32 v74, 0x3377d1cf, v79
	v_fmac_f32_e32 v74, 0x3f317217, v79
	v_add_f32_dpp v151, v151, v151 row_shr:4 row_mask:0xf bank_mask:0xf bound_ctrl:1
	v_add_f32_dpp v152, v152, v152 row_shr:4 row_mask:0xf bank_mask:0xf bound_ctrl:1
	v_sub_f32_e32 v79, 1.0, v203
	v_fma_f32 v75, v78, v79, v203
	v_max_f32_e32 v75, 0xda24260, v75
	v_sub_f32_e32 v161, 1.0, v75
	v_mov_b32_e32 v78, v75
	v_lshlrev_b32_e32 v75, 16, v0
	v_log_f32_e32 v78, v78
	v_mul_f32_e32 v75, 0xbfb8aa3b, v75
	v_exp_f32_e32 v75, v75
	v_mov_b32_e32 v160, v74
	v_mul_f32_e32 v74, 0x3f317217, v78
	v_fma_f32 v74, v78, s93, -v74
	v_add_f32_e32 v75, 1.0, v75
	v_fmac_f32_e32 v74, 0x3377d1cf, v78
	v_rcp_f32_e32 v75, v75
	v_fmac_f32_e32 v74, 0x3f317217, v78
	v_and_b32_e32 v0, 0xffff0000, v0
	v_mul_f32_e32 v0, 0xbfb8aa3b, v0
	v_mov_b32_e32 v162, v74
	v_sub_f32_e32 v74, 1.0, v204
	v_fma_f32 v68, v75, v74, v204
	v_max_f32_e32 v68, 0xda24260, v68
	v_exp_f32_e32 v0, v0
	v_lshlrev_b32_e32 v75, 16, v1
	v_log_f32_e32 v74, v68
	v_add_f32_e32 v0, 1.0, v0
	v_rcp_f32_e32 v0, v0
	v_and_b32_e32 v1, 0xffff0000, v1
	v_mul_f32_e32 v78, 0x3f317217, v74
	v_fma_f32 v78, v74, s93, -v78
	v_fmac_f32_e32 v78, 0x3377d1cf, v74
	v_fmac_f32_e32 v78, 0x3f317217, v74
	v_mul_f32_e32 v1, 0xbfb8aa3b, v1
	v_exp_f32_e32 v1, v1
	v_mov_b32_e32 v74, v78
	v_sub_f32_e32 v78, 1.0, v205
	v_fma_f32 v0, v0, v78, v205
	v_max_f32_e32 v0, 0xda24260, v0
	v_mov_b32_e32 v163, v74
	v_mul_f32_e32 v74, 0xbfb8aa3b, v75
	v_log_f32_e32 v69, v0
	v_exp_f32_e32 v74, v74
	v_sub_f32_e32 v164, 1.0, v0
	v_add_f32_e32 v1, 1.0, v1
	v_mul_f32_e32 v0, 0x3f317217, v69
	v_add_f32_e32 v74, 1.0, v74
	v_fma_f32 v0, v69, s93, -v0
	v_rcp_f32_e32 v74, v74
	v_fmac_f32_e32 v0, 0x3377d1cf, v69
	v_fmac_f32_e32 v0, 0x3f317217, v69
	v_rcp_f32_e32 v1, v1
	v_mov_b32_e32 v75, v148
	v_sub_f32_e32 v69, 1.0, v206
	v_fma_f32 v69, v74, v69, v206
	v_max_f32_e32 v69, 0xda24260, v69
; #define LAS __attribute__((address_space(3)))
; __device__ __forceinline__ float sigmoidf_(float x) { return __builtin_amdgcn_rcpf(1.0f + __expf(-x)); }
; template <int CTRL> __device__ __forceinline__ float dpp_add0(float x) { return x + dppf<CTRL>(0.0f, x); }
; template <bool WITHO, bool RAW = false>
; __device__ __forceinline__ void hg_pass(const Frame& F, const bf16_t* P, const float* lbh, int b, int h, int nb, int dir, f32x4 (&S)[4][4], float (&Gsum)[16],
;                                         LAS bf16_t* Vl, LAS bf16_t* Kl, float* OF, const float* ngp) {
;     ...
;         for (int m = 0; m < 4; ++m) { const float z0 = __uint_as_float(zr[m].x << 16), z1 = __uint_as_float(zr[m].x & 0xffff0000u), z2 = __uint_as_float(zr[m].y << 16), z3 = __uint_as_float(zr[m].y & 0xffff0000u);
;             const float zz[4] = {z0, z1, z2, z3};
;             const f32x4 lb4 = *(const f32x4*)(lbh + 16 * m + 4 * g);
; #pragma unroll
;             for (int i = 0; i < 4; ++i) { const float lb = lb4[i]; const float f = fmaxf(lb + (1.0f - lb) * sigmoidf_(zz[i]), 1e-30f); kk[m * 4 + i] = 1.0f - f; c[m * 4 + i] = __logf(f); }
;             *(LAS u32x2*)(Vl + tau * 64 + 16 * m + 4 * g) = vr[m];
;  }
;         if (ci + 1 < HG_U / 16) { const int pos = (ci + 1) * 16 + tau, t = dir ? (HG_U - 1 - pos) : pos; const bf16_t* pr = P + (size_t)hg_row(b, nb, t) * 4096 + h * 64 + 4 * g;
; #pragma unroll
;             for (int m = 0; m < 4; ++m) { zr[m] = *(const u32x2*)(pr + (dir ? 2560 : 2048) + 16 * m); vr[m] = *(const u32x2*)(pr + 3072 + 16 * m); } }
;         float G[16];
; #pragma unroll
;         for (int q = 0; q < 16; ++q) G[q] = c[q];
; #pragma unroll
;         for (int q = 0; q < 16; q += 4) ROW_ALLREDUCE4(G[q], G[q + 1], G[q + 2], G[q + 3]);
; #pragma unroll
;         for (int q = 0; q < 16; ++q) { c[q] = dpp_add0<0x111>(c[q]); c[q] = dpp_add0<0x112>(c[q]); c[q] = dpp_add0<0x114>(c[q]); c[q] = dpp_add0<0x118>(c[q]); }
; #pragma unroll
;         for (int q = 0; q < 16; ++q) Gsum[q] += G[q];
	v_log_f32_e32 v70, v69
	v_mov_b32_e32 v132, v0
	v_add_f32_dpp v0, v0, v0 row_shr:1 row_mask:0xf bank_mask:0xf bound_ctrl:1
	v_add_f32_dpp v148, v148, v148 row_shr:1 row_mask:0xf bank_mask:0xf bound_ctrl:1
	v_mul_f32_e32 v74, 0x3f317217, v70
	v_fma_f32 v74, v70, s93, -v74
	v_fmac_f32_e32 v74, 0x3377d1cf, v70
	v_fmac_f32_e32 v74, 0x3f317217, v70
	v_add_f32_dpp v0, v0, v0 row_shr:2 row_mask:0xf bank_mask:0xf bound_ctrl:1
	v_mov_b32_e32 v78, v83
	v_mov_b32_e32 v70, v74
	v_sub_f32_e32 v74, 1.0, v207
	v_fma_f32 v71, v1, v74, v207
	v_max_f32_e32 v1, 0xda24260, v71
	v_sub_f32_e32 v166, 1.0, v1
	v_log_f32_e32 v71, v1
	v_mov_b32_e32 v165, v70
	v_add_f32_dpp v0, v0, v0 row_shr:4 row_mask:0xf bank_mask:0xf bound_ctrl:1
	v_mul_f32_e32 v1, 0x3f317217, v71
	v_fma_f32 v1, v71, s93, -v1
	v_fmac_f32_e32 v1, 0x3377d1cf, v71
	v_fmac_f32_e32 v1, 0x3f317217, v71
	v_add_f32_dpp v167, v0, v0 row_shr:8 row_mask:0xf bank_mask:0xf bound_ctrl:1
	v_add_f32_dpp v0, v165, v165 row_shr:1 row_mask:0xf bank_mask:0xf bound_ctrl:1
	s_nop 1
	v_add_f32_dpp v0, v0, v0 row_shr:2 row_mask:0xf bank_mask:0xf bound_ctrl:1
	v_mov_b32_e32 v74, v149
	v_add_f32_dpp v149, v149, v149 row_shr:1 row_mask:0xf bank_mask:0xf bound_ctrl:1
	v_add_f32_dpp v0, v0, v0 row_shr:4 row_mask:0xf bank_mask:0xf bound_ctrl:1
	v_mov_b32_e32 v79, v150
	v_mov_b32_e32 v131, v165
	v_add_f32_dpp v148, v148, v148 row_shr:2 row_mask:0xf bank_mask:0xf bound_ctrl:1
	v_add_f32_dpp v149, v149, v149 row_shr:2 row_mask:0xf bank_mask:0xf bound_ctrl:1
	v_add_f32_dpp v150, v150, v150 row_shr:1 row_mask:0xf bank_mask:0xf bound_ctrl:1
	v_add_f32_dpp v83, v83, v83 row_shr:1 row_mask:0xf bank_mask:0xf bound_ctrl:1
	v_add_f32_dpp v165, v0, v0 row_shr:8 row_mask:0xf bank_mask:0xf bound_ctrl:1
	v_add_f32_dpp v0, v1, v1 row_shr:1 row_mask:0xf bank_mask:0xf bound_ctrl:1
	v_add_f32_dpp v148, v148, v148 row_shr:4 row_mask:0xf bank_mask:0xf bound_ctrl:1
	v_add_f32_dpp v149, v149, v149 row_shr:4 row_mask:0xf bank_mask:0xf bound_ctrl:1
	v_add_f32_dpp v150, v150, v150 row_shr:2 row_mask:0xf bank_mask:0xf bound_ctrl:1
	v_add_f32_dpp v83, v83, v83 row_shr:2 row_mask:0xf bank_mask:0xf bound_ctrl:1
	v_add_f32_dpp v0, v0, v0 row_shr:2 row_mask:0xf bank_mask:0xf bound_ctrl:1
	v_add_f32_dpp v148, v148, v148 row_shr:8 row_mask:0xf bank_mask:0xf bound_ctrl:1
	v_add_f32_dpp v149, v149, v149 row_shr:8 row_mask:0xf bank_mask:0xf bound_ctrl:1
	v_add_f32_dpp v150, v150, v150 row_shr:4 row_mask:0xf bank_mask:0xf bound_ctrl:1
	v_add_f32_dpp v83, v83, v83 row_shr:4 row_mask:0xf bank_mask:0xf bound_ctrl:1
	v_add_f32_dpp v0, v0, v0 row_shr:4 row_mask:0xf bank_mask:0xf bound_ctrl:1
	s_nop 1
	v_add_f32_dpp v75, v75, v75 quad_perm:[1,0,3,2] row_mask:0xf bank_mask:0xf
	v_add_f32_dpp v74, v74, v74 quad_perm:[1,0,3,2] row_mask:0xf bank_mask:0xf
	v_add_f32_dpp v79, v79, v79 quad_perm:[1,0,3,2] row_mask:0xf bank_mask:0xf
	v_add_f32_dpp v78, v78, v78 quad_perm:[1,0,3,2] row_mask:0xf bank_mask:0xf
	v_add_f32_dpp v75, v75, v75 quad_perm:[2,3,0,1] row_mask:0xf bank_mask:0xf
	v_add_f32_dpp v74, v74, v74 quad_perm:[2,3,0,1] row_mask:0xf bank_mask:0xf
	v_add_f32_dpp v79, v79, v79 quad_perm:[2,3,0,1] row_mask:0xf bank_mask:0xf
	v_add_f32_dpp v78, v78, v78 quad_perm:[2,3,0,1] row_mask:0xf bank_mask:0xf
	v_add_f32_dpp v75, v75, v75 row_half_mirror row_mask:0xf bank_mask:0xf
	v_add_f32_dpp v74, v74, v74 row_half_mirror row_mask:0xf bank_mask:0xf
	v_add_f32_dpp v79, v79, v79 row_half_mirror row_mask:0xf bank_mask:0xf
	v_add_f32_dpp v78, v78, v78 row_half_mirror row_mask:0xf bank_mask:0xf
	v_add_f32_dpp v75, v75, v75 row_mirror row_mask:0xf bank_mask:0xf
	v_add_f32_dpp v74, v74, v74 row_mirror row_mask:0xf bank_mask:0xf
	v_add_f32_dpp v79, v79, v79 row_mirror row_mask:0xf bank_mask:0xf
	v_add_f32_dpp v78, v78, v78 row_mirror row_mask:0xf bank_mask:0xf
	v_mov_b32_e32 v130, v1
	v_add_f32_dpp v150, v150, v150 row_shr:8 row_mask:0xf bank_mask:0xf bound_ctrl:1
	v_add_f32_dpp v83, v83, v83 row_shr:8 row_mask:0xf bank_mask:0xf bound_ctrl:1
	v_add_f32_dpp v168, v0, v0 row_shr:8 row_mask:0xf bank_mask:0xf bound_ctrl:1
	v_sub_f32_e32 v0, v75, v148
	v_sub_f32_e32 v1, v74, v149
	v_mul_f32_e32 v0, 0x3fb8aa3b, v0
	v_mul_f32_e32 v1, 0x3fb8aa3b, v1
	v_sub_f32_e32 v148, v79, v150
	v_sub_f32_e32 v83, v78, v83
	v_exp_f32_e32 v0, v0
	v_exp_f32_e32 v1, v1
	v_mul_f32_e32 v148, 0x3fb8aa3b, v148
	v_mul_f32_e32 v83, 0x3fb8aa3b, v83
	v_exp_f32_e32 v148, v148
	v_exp_f32_e32 v83, v83
	v_mov_b32_e32 v71, v154
	v_mov_b32_e32 v70, v156
	v_add_f32_dpp v154, v154, v154 row_shr:1 row_mask:0xf bank_mask:0xf bound_ctrl:1
	v_add_f32_dpp v156, v156, v156 row_shr:1 row_mask:0xf bank_mask:0xf bound_ctrl:1
	v_mov_b32_e32 v134, v162
	v_mov_b32_e32 v135, v160
	v_mov_b32_e32 v133, v163
	v_add_f32_dpp v154, v154, v154 row_shr:2 row_mask:0xf bank_mask:0xf bound_ctrl:1
	v_add_f32_dpp v156, v156, v156 row_shr:2 row_mask:0xf bank_mask:0xf bound_ctrl:1
	v_mul_f32_e32 v0, v3, v0
	v_mul_f32_e32 v1, v80, v1
	s_nop 1
	v_add_f32_dpp v139, v139, v139 quad_perm:[1,0,3,2] row_mask:0xf bank_mask:0xf
	v_add_f32_dpp v138, v138, v138 quad_perm:[1,0,3,2] row_mask:0xf bank_mask:0xf
	v_add_f32_dpp v71, v71, v71 quad_perm:[1,0,3,2] row_mask:0xf bank_mask:0xf
	v_add_f32_dpp v70, v70, v70 quad_perm:[1,0,3,2] row_mask:0xf bank_mask:0xf
	v_add_f32_dpp v139, v139, v139 quad_perm:[2,3,0,1] row_mask:0xf bank_mask:0xf
	v_add_f32_dpp v138, v138, v138 quad_perm:[2,3,0,1] row_mask:0xf bank_mask:0xf
	v_add_f32_dpp v71, v71, v71 quad_perm:[2,3,0,1] row_mask:0xf bank_mask:0xf
	v_add_f32_dpp v70, v70, v70 quad_perm:[2,3,0,1] row_mask:0xf bank_mask:0xf
	v_add_f32_dpp v139, v139, v139 row_half_mirror row_mask:0xf bank_mask:0xf
; #define LAS __attribute__((address_space(3)))
; __device__ __forceinline__ unsigned cvt_pk_bf16(float lo, float hi) { unsigned r; asm volatile("v_cvt_pk_bf16_f32 %0, %1, %2" : "=v"(r) : "v"(lo), "v"(hi)); return r; }
; template <int CTRL> __device__ __forceinline__ float dpp_add0(float x) { return x + dppf<CTRL>(0.0f, x); }
; template <bool WITHO, bool RAW = false>
; __device__ __forceinline__ void hg_pass(const Frame& F, const bf16_t* P, const float* lbh, int b, int h, int nb, int dir, f32x4 (&S)[4][4], float (&Gsum)[16],
;                                         LAS bf16_t* Vl, LAS bf16_t* Kl, float* OF, const float* ngp) {
;     ...
;         for (int q = 0; q < 16; q += 4) ROW_ALLREDUCE4(G[q], G[q + 1], G[q + 2], G[q + 3]);
; #pragma unroll
;         for (int q = 0; q < 16; ++q) { c[q] = dpp_add0<0x111>(c[q]); c[q] = dpp_add0<0x112>(c[q]); c[q] = dpp_add0<0x114>(c[q]); c[q] = dpp_add0<0x118>(c[q]); }
; #pragma unroll
;         for (int q = 0; q < 16; ++q) Gsum[q] += G[q];
; #pragma unroll
;         for (int m = 0; m < 4; ++m) { float kh[4];
; #pragma unroll
;             for (int i = 0; i < 4; ++i) kh[i] = kk[m * 4 + i] * __expf(G[m * 4 + i] - c[m * 4 + i]);
;             u32x2 w; w.x = cvt_pk_bf16(kh[0], kh[1]); w.y = cvt_pk_bf16(kh[2], kh[3]);
;             *(LAS u32x2*)(Kl + tau * 64 + 16 * m + 4 * g) = w; }
	v_add_f32_dpp v138, v138, v138 row_half_mirror row_mask:0xf bank_mask:0xf
	v_add_f32_dpp v71, v71, v71 row_half_mirror row_mask:0xf bank_mask:0xf
	v_add_f32_dpp v70, v70, v70 row_half_mirror row_mask:0xf bank_mask:0xf
	v_add_f32_dpp v139, v139, v139 row_mirror row_mask:0xf bank_mask:0xf
	v_add_f32_dpp v138, v138, v138 row_mirror row_mask:0xf bank_mask:0xf
	v_add_f32_dpp v71, v71, v71 row_mirror row_mask:0xf bank_mask:0xf
	v_add_f32_dpp v70, v70, v70 row_mirror row_mask:0xf bank_mask:0xf
	s_nop 1
	v_add_f32_dpp v137, v137, v137 quad_perm:[1,0,3,2] row_mask:0xf bank_mask:0xf
	v_add_f32_dpp v136, v136, v136 quad_perm:[1,0,3,2] row_mask:0xf bank_mask:0xf
	v_add_f32_dpp v135, v135, v135 quad_perm:[1,0,3,2] row_mask:0xf bank_mask:0xf
	v_add_f32_dpp v134, v134, v134 quad_perm:[1,0,3,2] row_mask:0xf bank_mask:0xf
	v_add_f32_dpp v137, v137, v137 quad_perm:[2,3,0,1] row_mask:0xf bank_mask:0xf
	v_add_f32_dpp v136, v136, v136 quad_perm:[2,3,0,1] row_mask:0xf bank_mask:0xf
	v_add_f32_dpp v135, v135, v135 quad_perm:[2,3,0,1] row_mask:0xf bank_mask:0xf
	v_add_f32_dpp v134, v134, v134 quad_perm:[2,3,0,1] row_mask:0xf bank_mask:0xf
	v_add_f32_dpp v137, v137, v137 row_half_mirror row_mask:0xf bank_mask:0xf
	v_add_f32_dpp v136, v136, v136 row_half_mirror row_mask:0xf bank_mask:0xf
	v_add_f32_dpp v135, v135, v135 row_half_mirror row_mask:0xf bank_mask:0xf
	v_add_f32_dpp v134, v134, v134 row_half_mirror row_mask:0xf bank_mask:0xf
	v_add_f32_dpp v137, v137, v137 row_mirror row_mask:0xf bank_mask:0xf
	v_add_f32_dpp v136, v136, v136 row_mirror row_mask:0xf bank_mask:0xf
	v_add_f32_dpp v135, v135, v135 row_mirror row_mask:0xf bank_mask:0xf
	v_add_f32_dpp v134, v134, v134 row_mirror row_mask:0xf bank_mask:0xf
	s_nop 1
	v_add_f32_dpp v133, v133, v133 quad_perm:[1,0,3,2] row_mask:0xf bank_mask:0xf
	v_add_f32_dpp v132, v132, v132 quad_perm:[1,0,3,2] row_mask:0xf bank_mask:0xf
	v_add_f32_dpp v131, v131, v131 quad_perm:[1,0,3,2] row_mask:0xf bank_mask:0xf
	v_add_f32_dpp v130, v130, v130 quad_perm:[1,0,3,2] row_mask:0xf bank_mask:0xf
	v_add_f32_dpp v133, v133, v133 quad_perm:[2,3,0,1] row_mask:0xf bank_mask:0xf
	v_add_f32_dpp v132, v132, v132 quad_perm:[2,3,0,1] row_mask:0xf bank_mask:0xf
	v_add_f32_dpp v131, v131, v131 quad_perm:[2,3,0,1] row_mask:0xf bank_mask:0xf
	v_add_f32_dpp v130, v130, v130 quad_perm:[2,3,0,1] row_mask:0xf bank_mask:0xf
	v_add_f32_dpp v133, v133, v133 row_half_mirror row_mask:0xf bank_mask:0xf
	v_add_f32_dpp v132, v132, v132 row_half_mirror row_mask:0xf bank_mask:0xf
	v_add_f32_dpp v131, v131, v131 row_half_mirror row_mask:0xf bank_mask:0xf
	v_add_f32_dpp v130, v130, v130 row_half_mirror row_mask:0xf bank_mask:0xf
	v_add_f32_dpp v133, v133, v133 row_mirror row_mask:0xf bank_mask:0xf
	v_add_f32_dpp v132, v132, v132 row_mirror row_mask:0xf bank_mask:0xf
	v_add_f32_dpp v131, v131, v131 row_mirror row_mask:0xf bank_mask:0xf
	v_add_f32_dpp v130, v130, v130 row_mirror row_mask:0xf bank_mask:0xf
	v_add_f32_dpp v151, v151, v151 row_shr:8 row_mask:0xf bank_mask:0xf bound_ctrl:1
	v_add_f32_dpp v152, v152, v152 row_shr:8 row_mask:0xf bank_mask:0xf bound_ctrl:1
	v_add_f32_dpp v154, v154, v154 row_shr:4 row_mask:0xf bank_mask:0xf bound_ctrl:1
	v_add_f32_dpp v156, v156, v156 row_shr:4 row_mask:0xf bank_mask:0xf bound_ctrl:1
	v_mul_f32_e32 v3, v81, v148
	v_mul_f32_e32 v80, v82, v83
	v_cvt_pk_bf16_f32 v0, v0, v1
	v_cvt_pk_bf16_f32 v1, v3, v80
	v_add_f32_dpp v154, v154, v154 row_shr:8 row_mask:0xf bank_mask:0xf bound_ctrl:1
	v_add_f32_dpp v156, v156, v156 row_shr:8 row_mask:0xf bank_mask:0xf bound_ctrl:1
	ds_write_b64 v143, v[0:1] offset:34816
	v_sub_f32_e32 v0, v139, v151
	v_sub_f32_e32 v1, v138, v152
	v_mul_f32_e32 v0, 0x3fb8aa3b, v0
	v_mul_f32_e32 v1, 0x3fb8aa3b, v1
	v_sub_f32_e32 v3, v71, v154
	v_sub_f32_e32 v80, v70, v156
	v_exp_f32_e32 v0, v0
	v_exp_f32_e32 v1, v1
	v_mul_f32_e32 v3, 0x3fb8aa3b, v3
	v_mul_f32_e32 v80, 0x3fb8aa3b, v80
	v_exp_f32_e32 v3, v3
	v_exp_f32_e32 v80, v80
	v_add_f32_dpp v157, v157, v157 row_shr:1 row_mask:0xf bank_mask:0xf bound_ctrl:1
	v_add_f32_dpp v158, v158, v158 row_shr:1 row_mask:0xf bank_mask:0xf bound_ctrl:1
	v_sub_f32_e32 v77, 1.0, v77
	v_add_f32_dpp v157, v157, v157 row_shr:2 row_mask:0xf bank_mask:0xf bound_ctrl:1
	v_add_f32_dpp v158, v158, v158 row_shr:2 row_mask:0xf bank_mask:0xf bound_ctrl:1
	v_add_f32_dpp v160, v160, v160 row_shr:1 row_mask:0xf bank_mask:0xf bound_ctrl:1
	v_add_f32_dpp v162, v162, v162 row_shr:1 row_mask:0xf bank_mask:0xf bound_ctrl:1
	v_add_f32_dpp v157, v157, v157 row_shr:4 row_mask:0xf bank_mask:0xf bound_ctrl:1
	v_add_f32_dpp v158, v158, v158 row_shr:4 row_mask:0xf bank_mask:0xf bound_ctrl:1
	v_add_f32_dpp v160, v160, v160 row_shr:2 row_mask:0xf bank_mask:0xf bound_ctrl:1
	v_add_f32_dpp v162, v162, v162 row_shr:2 row_mask:0xf bank_mask:0xf bound_ctrl:1
	v_mul_f32_e32 v0, v76, v0
	v_mul_f32_e32 v1, v77, v1
	v_add_f32_dpp v157, v157, v157 row_shr:8 row_mask:0xf bank_mask:0xf bound_ctrl:1
	v_add_f32_dpp v158, v158, v158 row_shr:8 row_mask:0xf bank_mask:0xf bound_ctrl:1
	v_add_f32_dpp v160, v160, v160 row_shr:4 row_mask:0xf bank_mask:0xf bound_ctrl:1
	v_add_f32_dpp v162, v162, v162 row_shr:4 row_mask:0xf bank_mask:0xf bound_ctrl:1
	v_mul_f32_e32 v3, v153, v3
	v_mul_f32_e32 v76, v155, v80
	v_cvt_pk_bf16_f32 v0, v0, v1
	v_cvt_pk_bf16_f32 v1, v3, v76
	v_add_f32_dpp v160, v160, v160 row_shr:8 row_mask:0xf bank_mask:0xf bound_ctrl:1
	v_add_f32_dpp v162, v162, v162 row_shr:8 row_mask:0xf bank_mask:0xf bound_ctrl:1
	ds_write_b64 v143, v[0:1] offset:34848
	v_sub_f32_e32 v0, v137, v157
	v_sub_f32_e32 v1, v136, v158
	v_mul_f32_e32 v0, 0x3fb8aa3b, v0
	v_mul_f32_e32 v1, 0x3fb8aa3b, v1
	v_sub_f32_e32 v3, v135, v160
; template <bool WITHO, bool RAW = false>
; __device__ __forceinline__ void hg_pass(const Frame& F, const bf16_t* P, const float* lbh, int b, int h, int nb, int dir, f32x4 (&S)[4][4], float (&Gsum)[16],
;                                         LAS bf16_t* Vl, LAS bf16_t* Kl, float* OF, const float* ngp) {
;     ...
;         asm volatile("s_waitcnt lgkmcnt(0)" ::: "memory");
;         u32x2 vtr[4], ktr[4];
;         asm volatile("ds_read_b64_tr_b16 %0, %8\n\tds_read_b64_tr_b16 %1, %8 offset:32\n\tds_read_b64_tr_b16 %2, %8 offset:64\n\tds_read_b64_tr_b16 %3, %8 offset:96\n\t"
;                      "ds_read_b64_tr_b16 %4, %9\n\tds_read_b64_tr_b16 %5, %9 offset:32\n\tds_read_b64_tr_b16 %6, %9 offset:64\n\tds_read_b64_tr_b16 %7, %9 offset:96\n\ts_waitcnt lgkmcnt(0)"
;                      : "=&v"(vtr[0]), "=&v"(vtr[1]), "=&v"(vtr[2]), "=&v"(vtr[3]), "=&v"(ktr[0]), "=&v"(ktr[1]), "=&v"(ktr[2]), "=&v"(ktr[3]) : "v"(vaddr), "v"(kaddr) : "memory");
;         bf16x8 Vf[4], Kf[4];
; #pragma unroll
;         for (int q = 0; q < 4; ++q) { u32x4 w; w.x = vtr[q].x; w.y = vtr[q].y; w.z = 0u; w.w = 0u; __builtin_memcpy(&Vf[q], &w, 16); u32x4 w2; w2.x = ktr[q].x; w2.y = ktr[q].y; w2.z = 0u; w2.w = 0u; __builtin_memcpy(&Kf[q], &w2, 16); }
;     ...
; #pragma unroll
;         for (int kt = 0; kt < 4; ++kt) { f32x4 eg;
; #pragma unroll
;             for (int i = 0; i < 4; ++i) eg[i] = __expf(G[kt * 4 + i]);
; #pragma unroll
;             for (int vt = 0; vt < 4; ++vt) S[kt][vt] = __builtin_amdgcn_mfma_f32_16x16x32_bf16(Kf[kt], Vf[vt], S[kt][vt] * eg, 0, 0, 0); }
	v_sub_f32_e32 v76, v134, v162
	v_exp_f32_e32 v0, v0
	v_exp_f32_e32 v1, v1
	v_mul_f32_e32 v3, 0x3fb8aa3b, v3
	v_mul_f32_e32 v76, 0x3fb8aa3b, v76
	v_exp_f32_e32 v3, v3
	v_exp_f32_e32 v76, v76
	v_add_f32_dpp v163, v163, v163 row_shr:1 row_mask:0xf bank_mask:0xf bound_ctrl:1
	v_sub_f32_e32 v72, 1.0, v72
	v_sub_f32_e32 v73, 1.0, v73
	v_add_f32_dpp v163, v163, v163 row_shr:2 row_mask:0xf bank_mask:0xf bound_ctrl:1
	v_pk_add_f32 v[108:109], v[108:109], v[74:75]
	v_mul_f32_e32 v75, 0x3fb8aa3b, v75
	v_add_f32_dpp v163, v163, v163 row_shr:4 row_mask:0xf bank_mask:0xf bound_ctrl:1
	v_mul_f32_e32 v0, v72, v0
	v_mul_f32_e32 v1, v73, v1
	v_exp_f32_e32 v150, v75
	v_mul_f32_e32 v74, 0x3fb8aa3b, v74
	v_mul_f32_e32 v75, 0x3fb8aa3b, v79
	v_add_f32_dpp v163, v163, v163 row_shr:8 row_mask:0xf bank_mask:0xf bound_ctrl:1
	v_mul_f32_e32 v3, v159, v3
	v_mul_f32_e32 v72, v161, v76
	v_cvt_pk_bf16_f32 v0, v0, v1
	v_cvt_pk_bf16_f32 v1, v3, v72
	v_exp_f32_e32 v160, v75
	v_mul_f32_e32 v75, 0x3fb8aa3b, v78
	v_exp_f32_e32 v151, v74
	ds_write_b64 v143, v[0:1] offset:34880
	v_sub_f32_e32 v0, v133, v163
	v_sub_f32_e32 v1, v132, v167
	v_exp_f32_e32 v161, v75
	v_mul_f32_e32 v0, 0x3fb8aa3b, v0
	v_mul_f32_e32 v1, 0x3fb8aa3b, v1
	v_sub_f32_e32 v3, v131, v165
	v_sub_f32_e32 v72, v130, v168
	v_exp_f32_e32 v0, v0
	v_exp_f32_e32 v1, v1
	v_mul_f32_e32 v3, 0x3fb8aa3b, v3
	v_mul_f32_e32 v72, 0x3fb8aa3b, v72
	v_exp_f32_e32 v3, v3
	v_exp_f32_e32 v72, v72
	v_pk_mul_f32 v[64:65], v[64:65], v[150:151]
	v_pk_mul_f32 v[60:61], v[60:61], v[150:151]
	v_pk_mul_f32 v[52:53], v[52:53], v[150:151]
	v_pk_mul_f32 v[56:57], v[56:57], v[150:151]
	v_mul_f32_e32 v150, 0x3fb8aa3b, v139
	v_mul_f32_e32 v151, 0x3fb8aa3b, v71
	v_pk_mul_f32 v[66:67], v[66:67], v[160:161]
	v_pk_mul_f32 v[62:63], v[62:63], v[160:161]
	v_pk_mul_f32 v[54:55], v[54:55], v[160:161]
	v_pk_mul_f32 v[58:59], v[58:59], v[160:161]
	v_exp_f32_e32 v160, v150
	v_mul_f32_e32 v150, 0x3fb8aa3b, v138
	v_exp_f32_e32 v162, v151
	v_mul_f32_e32 v151, 0x3fb8aa3b, v70
	v_sub_f32_e32 v68, 1.0, v68
	v_mov_b32_e32 v158, v2
	v_mov_b32_e32 v159, v2
	v_mov_b32_e32 v154, v2
	v_mov_b32_e32 v155, v2
	v_exp_f32_e32 v163, v151
	v_exp_f32_e32 v161, v150
	v_pk_add_f32 v[104:105], v[104:105], v[138:139]
	v_mul_f32_e32 v138, 0x3fb8aa3b, v137
	v_mul_f32_e32 v139, 0x3fb8aa3b, v136
	v_sub_f32_e32 v69, 1.0, v69
	v_mul_f32_e32 v0, v68, v0
	v_mul_f32_e32 v1, v164, v1
	v_exp_f32_e32 v138, v138
	v_exp_f32_e32 v139, v139
	v_mul_f32_e32 v3, v69, v3
	v_mul_f32_e32 v68, v166, v72
	v_cvt_pk_bf16_f32 v0, v0, v1
	v_cvt_pk_bf16_f32 v1, v3, v68
	ds_write_b64 v143, v[0:1] offset:34912
	s_waitcnt lgkmcnt(0)
	v_pk_add_f32 v[106:107], v[106:107], v[78:79]
	ds_read_b64_tr_b16 v[0:1], v140
	ds_read_b64_tr_b16 v[80:81], v140 offset:32
	ds_read_b64_tr_b16 v[76:77], v140 offset:64
	ds_read_b64_tr_b16 v[72:73], v140 offset:96
	ds_read_b64_tr_b16 v[156:157], v141
	ds_read_b64_tr_b16 v[152:153], v141 offset:32
	ds_read_b64_tr_b16 v[148:149], v141 offset:64
	ds_read_b64_tr_b16 v[68:69], v141 offset:96
	s_waitcnt lgkmcnt(0)
	v_mov_b32_e32 v3, v2
	v_mov_b32_e32 v82, v2
	v_mov_b32_e32 v83, v2
	v_mov_b32_e32 v78, v2
	v_mov_b32_e32 v79, v2
	v_mov_b32_e32 v74, v2
	v_mov_b32_e32 v75, v2
	v_pk_mul_f32 v[50:51], v[50:51], v[162:163]
	v_pk_mul_f32 v[48:49], v[48:49], v[160:161]
	v_pk_mul_f32 v[46:47], v[46:47], v[162:163]
	v_pk_mul_f32 v[44:45], v[44:45], v[160:161]
	v_pk_mul_f32 v[38:39], v[38:39], v[162:163]
	v_pk_mul_f32 v[36:37], v[36:37], v[160:161]
	v_pk_mul_f32 v[42:43], v[42:43], v[162:163]
	v_pk_mul_f32 v[40:41], v[40:41], v[160:161]
	v_mfma_f32_16x16x32_bf16 v[64:67], v[156:159], v[0:3], v[64:67]
	v_mul_f32_e64 v32, v32, v138
	v_mul_f32_e64 v33, v33, v139
	v_pk_mul_f32 v[28:29], v[28:29], v[138:139]
	v_pk_mul_f32 v[20:21], v[20:21], v[138:139]
	v_mfma_f32_16x16x32_bf16 v[60:63], v[156:159], v[80:83], v[60:63]
	v_mul_f32_e64 v24, v24, v138
	v_mul_f32_e64 v25, v25, v139
	v_mul_f32_e32 v138, 0x3fb8aa3b, v133
	v_mul_f32_e32 v139, 0x3fb8aa3b, v132
	v_mfma_f32_16x16x32_bf16 v[52:55], v[156:159], v[76:79], v[52:55]
	v_mov_b32_e32 v150, v2
	v_mov_b32_e32 v151, v2
	v_pk_add_f32 v[102:103], v[102:103], v[70:71]
	v_mfma_f32_16x16x32_bf16 v[56:59], v[156:159], v[72:75], v[56:59]
	v_mul_f32_e32 v156, 0x3fb8aa3b, v135
	v_mul_f32_e32 v157, 0x3fb8aa3b, v134
	v_exp_f32_e32 v156, v156
	v_mfma_f32_16x16x32_bf16 v[48:51], v[152:155], v[0:3], v[48:51]
	v_exp_f32_e32 v157, v157
	v_mov_b32_e32 v70, v2
	v_mov_b32_e32 v71, v2
	v_mfma_f32_16x16x32_bf16 v[44:47], v[152:155], v[80:83], v[44:47]
	v_exp_f32_e32 v138, v138
	v_exp_f32_e32 v139, v139
	v_pk_mul_f32 v[34:35], v[34:35], v[156:157]
	v_mfma_f32_16x16x32_bf16 v[36:39], v[152:155], v[76:79], v[36:39]
	v_mul_f32_e64 v30, v30, v156
	v_mul_f32_e64 v31, v31, v157
	v_pk_mul_f32 v[22:23], v[22:23], v[156:157]
	v_pk_mul_f32 v[26:27], v[26:27], v[156:157]
	v_mfma_f32_16x16x32_bf16 v[40:43], v[152:155], v[72:75], v[40:43]
	v_mul_f32_e32 v152, 0x3fb8aa3b, v131
	v_mul_f32_e32 v153, 0x3fb8aa3b, v130
	v_exp_f32_e32 v152, v152
	v_exp_f32_e32 v153, v153
	v_pk_mul_f32 v[16:17], v[16:17], v[138:139]
	v_pk_mul_f32 v[12:13], v[12:13], v[138:139]
	v_pk_mul_f32 v[8:9], v[8:9], v[138:139]
	v_pk_mul_f32 v[18:19], v[18:19], v[152:153]
	v_pk_mul_f32 v[14:15], v[14:15], v[152:153]
	v_pk_mul_f32 v[10:11], v[10:11], v[152:153]
	v_pk_mul_f32 v[6:7], v[6:7], v[152:153]
	v_pk_mul_f32 v[4:5], v[4:5], v[138:139]
	v_mfma_f32_16x16x32_bf16 v[32:35], v[148:151], v[0:3], v[32:35]
	v_add_f32_e64 v100, v100, v136
	v_add_f32_e64 v101, v101, v137
	v_pk_add_f32 v[98:99], v[98:99], v[134:135]
	v_pk_add_f32 v[96:97], v[96:97], v[132:133]
	v_mfma_f32_16x16x32_bf16 v[28:31], v[148:151], v[80:83], v[28:31]
	v_add_f32_e64 v94, v94, v130
	v_add_f32_e64 v95, v95, v131
	s_waitcnt vmcnt(0)
	v_mov_b64_e32 v[134:135], v[122:123]
	v_mov_b64_e32 v[132:133], v[124:125]
	v_mfma_f32_16x16x32_bf16 v[20:23], v[148:151], v[76:79], v[20:23]
	v_mov_b64_e32 v[130:131], v[126:127]
	v_mfma_f32_16x16x32_bf16 v[24:27], v[148:151], v[72:75], v[24:27]
	v_mfma_f32_16x16x32_bf16 v[16:19], v[68:71], v[0:3], v[16:19]
	v_mov_b64_e32 v[0:1], v[128:129]
	v_mfma_f32_16x16x32_bf16 v[12:15], v[68:71], v[80:83], v[12:15]
	v_mfma_f32_16x16x32_bf16 v[8:11], v[68:71], v[76:79], v[8:11]
	v_mfma_f32_16x16x32_bf16 v[4:7], v[68:71], v[72:75], v[4:7]
	s_cbranch_scc0 .LBB0_692
; #define LAS __attribute__((address_space(3)))
; template <bool WITHO, bool RAW = false>
; __device__ __forceinline__ void hg_pass(const Frame& F, const bf16_t* P, const float* lbh, int b, int h, int nb, int dir, f32x4 (&S)[4][4], float (&Gsum)[16],
;                                         LAS bf16_t* Vl, LAS bf16_t* Kl, float* OF, const float* ngp) {
;     ...
;             *(LAS u32x2*)(Vl + tau * 64 + 16 * m + 4 * g) = vr[m];
;  }
;         if (ci + 1 < HG_U / 16) { const int pos = (ci + 1) * 16 + tau, t = dir ? (HG_U - 1 - pos) : pos; const bf16_t* pr = P + (size_t)hg_row(b, nb, t) * 4096 + h * 64 + 4 * g;
; #pragma unroll
;             for (int m = 0; m < 4; ++m) { zr[m] = *(const u32x2*)(pr + (dir ? 2560 : 2048) + 16 * m); vr[m] = *(const u32x2*)(pr + 3072 + 16 * m); } }
.LBB0_690:
	v_add_u32_e32 v3, 0x8000, v143
	s_cmp_eq_u32 s5, -1
	ds_write2_b64 v3, v[114:115], v[116:117] offset1:4
	ds_write2_b64 v3, v[118:119], v[120:121] offset0:8 offset1:12
	s_cbranch_scc1 .LBB0_689
	v_add_u32_e32 v3, s5, v146
	v_cndmask_b32_e64 v3, v3, v147, s[36:37]
	v_add_u32_e32 v114, s4, v3
	v_ashrrev_i32_e32 v115, 31, v114
	v_lshlrev_b64 v[114:115], 13, v[114:115]
	v_lshl_add_u64 v[114:115], v[112:113], 0, v[114:115]
	v_add_co_u32_e32 v120, vcc, 0x1000, v114
	v_lshl_add_u64 v[116:117], v[114:115], 0, s[64:65]
	s_nop 0
	v_addc_co_u32_e32 v121, vcc, 0, v115, vcc
	global_load_dwordx2 v[122:123], v[116:117], off
	global_load_dwordx2 v[124:125], v[116:117], off offset:32
	global_load_dwordx2 v[126:127], v[116:117], off offset:64
	global_load_dwordx2 v[128:129], v[116:117], off offset:96
	global_load_dwordx2 v[114:115], v[120:121], off offset:2048
	s_nop 0
	global_load_dwordx2 v[116:117], v[120:121], off offset:2080
	global_load_dwordx2 v[118:119], v[120:121], off offset:2112
	s_nop 0
	global_load_dwordx2 v[120:121], v[120:121], off offset:2144
	s_branch .LBB0_689
